# final RMSNorm phase output stores made write-through (sc1) so the end-of-kernel L2 writeback has nothing left to flush
# speedup vs baseline: 1.0359x; 1.0062x over previous
; __device__ __forceinline__ float f16_lo(unsigned u) { return (float)__builtin_bit_cast(h16x2, u)[0]; }
; __device__ __forceinline__ float f16_hi(unsigned u) { return (float)__builtin_bit_cast(h16x2, u)[1]; }
; #define GAS __attribute__((address_space(1)))
; __global__ void __launch_bounds__(NWAVES * 64, 2) mk_fwd(Args args) {
;     ...
;         { int m = gw; asm volatile("" : "+s"(m)); const GAS f32x4* gr = (const GAS f32x4*)ap->in[22] + ln;
;           for (; m < M; m += 2 * NGW) { f32x4 v[2][4]; float ss[2] = {0.f, 0.f};
; #pragma unroll
;               for (int r = 0; r < 2; ++r) { const GAS v2u* xr = (const GAS v2u*)(hx + (size_t)(m + r * NGW) * D) + ln;
; #pragma unroll
;                   for (int q = 0; q < 4; ++q) { const v2u hv = xr[64 * q]; v[r][q] = (f32x4){pg8::f16_lo(hv.x), pg8::f16_hi(hv.x), pg8::f16_lo(hv.y), pg8::f16_hi(hv.y)}; } }
; #pragma unroll
;               for (int r = 0; r < 2; ++r) {
; #pragma unroll
;                   for (int q = 0; q < 4; ++q) ss[r] += (v[r][q].x * v[r][q].x + v[r][q].y * v[r][q].y) + (v[r][q].z * v[r][q].z + v[r][q].w * v[r][q].w);
;                   const float rstd = rsqrtf(wave_sum(ss[r], ln) * (1.f / D) + EPS); GAS f32x4* o = (GAS f32x4*)(ap->out + (size_t)(m + r * NGW) * D) + ln;
; #pragma unroll
;                   for (int q = 0; q < 4; ++q) o[64 * q] = v[r][q] * rstd * gr[64 * q]; } } }
.LBB0_1358:
	s_ashr_i32 s61, s60, 31
	s_lshl_b64 s[2:3], s[60:61], 11
	s_add_u32 s2, s1, s2
	s_addc_u32 s3, s4, s3
	v_lshl_add_u64 v[16:17], s[2:3], 0, v[4:5]
	global_load_dwordx2 v[20:21], v[16:17], off
	global_load_dwordx2 v[22:23], v[16:17], off offset:512
	global_load_dwordx2 v[24:25], v[16:17], off offset:1024
	s_add_i32 s2, s54, s60
	global_load_dwordx2 v[26:27], v[16:17], off offset:1536
	s_ashr_i32 s3, s2, 31
	s_lshl_b64 s[8:9], s[2:3], 11
	s_add_u32 s8, s1, s8
	s_addc_u32 s9, s4, s9
	v_lshl_add_u64 v[28:29], s[8:9], 0, v[4:5]
	global_load_dwordx2 v[30:31], v[28:29], off
	global_load_dwordx2 v[32:33], v[28:29], off offset:512
	global_load_dwordx2 v[34:35], v[28:29], off offset:1024
	global_load_dwordx2 v[36:37], v[28:29], off offset:1536
	global_load_dwordx2 v[38:39], v[0:1], off offset:184
	global_load_dwordx4 v[16:19], v[8:9], off
	s_lshl_b64 s[8:9], s[60:61], 12
	s_lshl_b64 s[2:3], s[2:3], 12
	s_add_i32 s60, s60, s5
	s_cmpk_lt_i32 s60, 0x4000
	s_waitcnt vmcnt(0)
	v_cvt_f32_f16_e32 v28, v20
	v_cvt_f32_f16_sdwa v29, v20 dst_sel:DWORD dst_unused:UNUSED_PAD src0_sel:WORD_1
	v_cvt_f32_f16_e32 v20, v21
	v_cvt_f32_f16_sdwa v21, v21 dst_sel:DWORD dst_unused:UNUSED_PAD src0_sel:WORD_1
	v_cvt_f32_f16_e32 v40, v22
	v_cvt_f32_f16_sdwa v41, v22 dst_sel:DWORD dst_unused:UNUSED_PAD src0_sel:WORD_1
	v_cvt_f32_f16_e32 v22, v23
	v_cvt_f32_f16_sdwa v23, v23 dst_sel:DWORD dst_unused:UNUSED_PAD src0_sel:WORD_1
	v_cvt_f32_f16_e32 v42, v24
	v_cvt_f32_f16_sdwa v43, v24 dst_sel:DWORD dst_unused:UNUSED_PAD src0_sel:WORD_1
	v_cvt_f32_f16_e32 v24, v25
	v_cvt_f32_f16_sdwa v25, v25 dst_sel:DWORD dst_unused:UNUSED_PAD src0_sel:WORD_1
	v_cvt_f32_f16_e32 v44, v26
	v_cvt_f32_f16_sdwa v45, v26 dst_sel:DWORD dst_unused:UNUSED_PAD src0_sel:WORD_1
	v_cvt_f32_f16_e32 v26, v27
	v_cvt_f32_f16_sdwa v27, v27 dst_sel:DWORD dst_unused:UNUSED_PAD src0_sel:WORD_1
	v_cvt_f32_f16_e32 v46, v30
	v_cvt_f32_f16_sdwa v47, v30 dst_sel:DWORD dst_unused:UNUSED_PAD src0_sel:WORD_1
	v_cvt_f32_f16_e32 v30, v31
	v_cvt_f32_f16_sdwa v31, v31 dst_sel:DWORD dst_unused:UNUSED_PAD src0_sel:WORD_1
	v_cvt_f32_f16_e32 v48, v32
	v_cvt_f32_f16_sdwa v49, v32 dst_sel:DWORD dst_unused:UNUSED_PAD src0_sel:WORD_1
	v_cvt_f32_f16_e32 v32, v33
	v_cvt_f32_f16_sdwa v33, v33 dst_sel:DWORD dst_unused:UNUSED_PAD src0_sel:WORD_1
	v_mov_b32_e32 v56, v29
	v_mov_b32_e32 v57, v21
	v_mov_b32_e32 v60, v41
	v_mov_b32_e32 v61, v23
	v_mov_b32_e32 v54, v28
	v_mov_b32_e32 v55, v20
	v_mov_b32_e32 v58, v40
	v_mov_b32_e32 v59, v22
	v_mul_f32_e32 v62, v43, v43
	v_mul_f32_e32 v64, v25, v25
	v_pk_mul_f32 v[56:57], v[56:57], v[56:57]
	v_pk_mul_f32 v[60:61], v[60:61], v[60:61]
	v_cvt_f32_f16_e32 v50, v34
	v_cvt_f32_f16_sdwa v51, v34 dst_sel:DWORD dst_unused:UNUSED_PAD src0_sel:WORD_1
	v_cvt_f32_f16_e32 v34, v35
	v_cvt_f32_f16_sdwa v35, v35 dst_sel:DWORD dst_unused:UNUSED_PAD src0_sel:WORD_1
	v_pk_mul_f32 v[68:69], v[26:27], v[26:27]
	v_pk_fma_f32 v[62:63], v[42:43], v[42:43], v[62:63] op_sel_hi:[1,1,0]
	v_pk_fma_f32 v[64:65], v[24:25], v[24:25], v[64:65] op_sel_hi:[1,1,0]
	v_pk_fma_f32 v[54:55], v[54:55], v[54:55], v[56:57]
	v_pk_fma_f32 v[56:57], v[58:59], v[58:59], v[60:61]
	v_cvt_f32_f16_e32 v52, v36
	v_cvt_f32_f16_sdwa v53, v36 dst_sel:DWORD dst_unused:UNUSED_PAD src0_sel:WORD_1
	v_cvt_f32_f16_e32 v36, v37
	v_cvt_f32_f16_sdwa v37, v37 dst_sel:DWORD dst_unused:UNUSED_PAD src0_sel:WORD_1
	v_pk_mul_f32 v[66:67], v[44:45], v[44:45]
	v_mov_b32_e32 v63, v68
	v_mov_b32_e32 v65, v69
	v_pk_add_f32 v[54:55], v[54:55], v[54:55] op_sel:[0,1] op_sel_hi:[1,0]
	v_pk_add_f32 v[56:57], v[56:57], v[56:57] op_sel:[0,1] op_sel_hi:[1,0]
	v_pk_add_f32 v[58:59], v[62:63], v[64:65]
	v_mov_b32_e32 v55, v66
	v_mov_b32_e32 v57, v67
	v_mov_b32_e32 v62, v47
	v_mov_b32_e32 v63, v31
	v_mov_b32_e32 v66, v49
	v_mov_b32_e32 v67, v33
	v_mov_b32_e32 v60, v46
	v_mov_b32_e32 v61, v30
	v_mov_b32_e32 v64, v48
	v_mov_b32_e32 v65, v32
	v_pk_add_f32 v[54:55], v[54:55], v[56:57]
	v_pk_mul_f32 v[56:57], v[62:63], v[62:63]
	v_pk_mul_f32 v[62:63], v[66:67], v[66:67]
	v_mul_f32_e32 v68, v51, v51
	v_mul_f32_e32 v70, v35, v35
	v_pk_add_f32 v[54:55], v[54:55], v[58:59]
	v_pk_fma_f32 v[56:57], v[60:61], v[60:61], v[56:57]
	v_pk_fma_f32 v[58:59], v[64:65], v[64:65], v[62:63]
	v_pk_fma_f32 v[66:67], v[50:51], v[50:51], v[68:69] op_sel_hi:[1,1,0]
	v_pk_add_f32 v[56:57], v[56:57], v[56:57] op_sel:[0,1] op_sel_hi:[1,0]
	v_pk_add_f32 v[58:59], v[58:59], v[58:59] op_sel:[0,1] op_sel_hi:[1,0]
	v_pk_fma_f32 v[60:61], v[34:35], v[34:35], v[70:71] op_sel_hi:[1,1,0]
	v_pk_mul_f32 v[62:63], v[52:53], v[52:53]
	v_pk_mul_f32 v[64:65], v[36:37], v[36:37]
	v_mov_b32_e32 v57, v62
	v_mov_b32_e32 v59, v63
	v_mov_b32_e32 v67, v64
	v_mov_b32_e32 v61, v65
	v_pk_add_f32 v[56:57], v[56:57], v[58:59]
	v_pk_add_f32 v[58:59], v[66:67], v[60:61]
	s_waitcnt lgkmcnt(0)
; #define GAS __attribute__((address_space(1)))
; __global__ void __launch_bounds__(NWAVES * 64, 2) mk_fwd(Args args) {
;     ...
;               for (int r = 0; r < 2; ++r) {
; #pragma unroll
;                   for (int q = 0; q < 4; ++q) ss[r] += (v[r][q].x * v[r][q].x + v[r][q].y * v[r][q].y) + (v[r][q].z * v[r][q].z + v[r][q].w * v[r][q].w);
;                   const float rstd = rsqrtf(wave_sum(ss[r], ln) * (1.f / D) + EPS); GAS f32x4* o = (GAS f32x4*)(ap->out + (size_t)(m + r * NGW) * D) + ln;
; #pragma unroll
;                   for (int q = 0; q < 4; ++q) o[64 * q] = v[r][q] * rstd * gr[64 * q]; } } }
	v_lshl_add_u64 v[38:39], v[38:39], 0, s[8:9]
	v_pk_add_f32 v[56:57], v[56:57], v[58:59]
	v_mov_b32_e32 v59, v54
	v_mov_b32_e32 v58, v56
	v_mov_b32_e32 v54, v57
	v_pk_add_f32 v[54:55], v[58:59], v[54:55]
	ds_bpermute_b32 v57, v3, v55
	ds_bpermute_b32 v56, v3, v54
	v_lshl_add_u64 v[38:39], v[38:39], 0, v[6:7]
	s_waitcnt lgkmcnt(0)
	v_pk_add_f32 v[54:55], v[54:55], v[56:57]
	ds_bpermute_b32 v57, v10, v55
	ds_bpermute_b32 v56, v10, v54
	s_waitcnt lgkmcnt(0)
	v_pk_add_f32 v[54:55], v[54:55], v[56:57]
	ds_bpermute_b32 v57, v11, v55
	ds_bpermute_b32 v56, v11, v54
	s_waitcnt lgkmcnt(0)
	v_pk_add_f32 v[54:55], v[54:55], v[56:57]
	ds_bpermute_b32 v57, v12, v55
	ds_bpermute_b32 v56, v12, v54
	s_waitcnt lgkmcnt(0)
	v_pk_add_f32 v[54:55], v[54:55], v[56:57]
	ds_bpermute_b32 v57, v13, v55
	ds_bpermute_b32 v56, v13, v54
	s_waitcnt lgkmcnt(0)
	v_pk_add_f32 v[54:55], v[54:55], v[56:57]
	ds_bpermute_b32 v57, v14, v55
	ds_bpermute_b32 v56, v14, v54
	s_waitcnt lgkmcnt(0)
	v_pk_add_f32 v[54:55], v[54:55], v[56:57]
	s_nop 0
	v_pk_fma_f32 v[54:55], v[54:55], s[0:1], v[2:3] op_sel_hi:[1,0,0]
	s_nop 0
	v_mul_f32_e32 v15, 0x4b800000, v55
	v_cmp_gt_f32_e32 vcc, s6, v55
	s_nop 1
	v_cndmask_b32_e32 v15, v55, v15, vcc
	v_rsq_f32_e32 v15, v15
	s_nop 0
	v_mul_f32_e32 v55, 0x45800000, v15
	v_cndmask_b32_e32 v56, v15, v55, vcc
	v_pk_mul_f32 v[28:29], v[56:57], v[28:29] op_sel_hi:[0,1]
	v_pk_mul_f32 v[20:21], v[56:57], v[20:21] op_sel_hi:[0,1]
	v_pk_mul_f32 v[18:19], v[20:21], v[18:19]
	v_pk_mul_f32 v[16:17], v[28:29], v[16:17]
	global_store_dwordx4 v[38:39], v[16:19], off sc1
	global_load_dwordx4 v[16:19], v[8:9], off offset:1024
	v_pk_mul_f32 v[20:21], v[56:57], v[22:23] op_sel_hi:[0,1]
	v_pk_mul_f32 v[22:23], v[56:57], v[40:41] op_sel_hi:[0,1]
	v_mul_f32_e32 v15, 0x4b800000, v54
	v_cmp_gt_f32_e32 vcc, s6, v54
	s_waitcnt vmcnt(0)
	v_pk_mul_f32 v[16:17], v[22:23], v[16:17]
	v_pk_mul_f32 v[18:19], v[20:21], v[18:19]
	global_store_dwordx4 v[38:39], v[16:19], off offset:1024 sc1
	global_load_dwordx4 v[16:19], v[8:9], off offset:2048
	v_pk_mul_f32 v[20:21], v[56:57], v[24:25] op_sel_hi:[0,1]
	v_pk_mul_f32 v[22:23], v[56:57], v[42:43] op_sel_hi:[0,1]
	v_cndmask_b32_e32 v15, v54, v15, vcc
	v_rsq_f32_e32 v15, v15
	s_waitcnt vmcnt(0)
	v_pk_mul_f32 v[16:17], v[22:23], v[16:17]
	v_pk_mul_f32 v[18:19], v[20:21], v[18:19]
	global_store_dwordx4 v[38:39], v[16:19], off offset:2048 sc1
	global_load_dwordx4 v[16:19], v[8:9], off offset:3072
	v_pk_mul_f32 v[20:21], v[56:57], v[26:27] op_sel_hi:[0,1]
	v_pk_mul_f32 v[22:23], v[56:57], v[44:45] op_sel_hi:[0,1]
	s_waitcnt vmcnt(0)
	v_pk_mul_f32 v[16:17], v[22:23], v[16:17]
	v_pk_mul_f32 v[18:19], v[20:21], v[18:19]
	global_store_dwordx4 v[38:39], v[16:19], off offset:3072 sc1
	global_load_dwordx2 v[20:21], v[0:1], off offset:184
	s_nop 0
	global_load_dwordx4 v[16:19], v[8:9], off
	v_mul_f32_e32 v22, 0x45800000, v15
	v_cndmask_b32_e32 v22, v15, v22, vcc
	v_pk_mul_f32 v[24:25], v[22:23], v[30:31] op_sel_hi:[0,1]
	v_pk_mul_f32 v[26:27], v[22:23], v[46:47] op_sel_hi:[0,1]
	s_waitcnt vmcnt(0) lgkmcnt(0)
	v_lshl_add_u64 v[20:21], v[20:21], 0, s[2:3]
	v_pk_mul_f32 v[16:17], v[26:27], v[16:17]
	v_pk_mul_f32 v[18:19], v[24:25], v[18:19]
	v_lshl_add_u64 v[20:21], v[20:21], 0, v[6:7]
	global_store_dwordx4 v[20:21], v[16:19], off sc1
	global_load_dwordx4 v[16:19], v[8:9], off offset:1024
	v_pk_mul_f32 v[24:25], v[22:23], v[32:33] op_sel_hi:[0,1]
	v_pk_mul_f32 v[26:27], v[22:23], v[48:49] op_sel_hi:[0,1]
	s_waitcnt vmcnt(0)
	v_pk_mul_f32 v[16:17], v[26:27], v[16:17]
	v_pk_mul_f32 v[18:19], v[24:25], v[18:19]
	global_store_dwordx4 v[20:21], v[16:19], off offset:1024 sc1
	global_load_dwordx4 v[16:19], v[8:9], off offset:2048
	v_pk_mul_f32 v[24:25], v[22:23], v[34:35] op_sel_hi:[0,1]
	v_pk_mul_f32 v[26:27], v[22:23], v[50:51] op_sel_hi:[0,1]
	s_waitcnt vmcnt(0)
	v_pk_mul_f32 v[16:17], v[26:27], v[16:17]
	v_pk_mul_f32 v[18:19], v[24:25], v[18:19]
	global_store_dwordx4 v[20:21], v[16:19], off offset:2048 sc1
	global_load_dwordx4 v[16:19], v[8:9], off offset:3072
	v_pk_mul_f32 v[24:25], v[22:23], v[36:37] op_sel_hi:[0,1]
	v_pk_mul_f32 v[22:23], v[22:23], v[52:53] op_sel_hi:[0,1]
	s_waitcnt vmcnt(0)
	v_pk_mul_f32 v[16:17], v[22:23], v[16:17]
	v_pk_mul_f32 v[18:19], v[24:25], v[18:19]
	global_store_dwordx4 v[20:21], v[16:19], off offset:3072 sc1
	s_cbranch_scc1 .LBB0_1358
